# layer1: MFMA steps 4-7 double-buffered (second fragment buffer = freed staging registers)
# speedup vs baseline: 1.0006x; 1.0006x over previous
.Lg1_final:
	v_max_i32_e32 v94, 1, v78
	v_cvt_f32_u32_e32 v94, v94
	v_div_scale_f32 v96, s[62:63], v94, v94, 1.0
	v_rcp_f32_e32 v97, v96
	v_div_scale_f32 v98, vcc, 1.0, v94, 1.0
	v_fma_f32 v99, -v96, v97, 1.0
	v_fmac_f32_e32 v97, v99, v97
	v_mul_f32_e32 v99, v98, v97
	v_fma_f32 v95, -v96, v99, v98
	v_fmac_f32_e32 v99, v95, v97
	v_fma_f32 v96, -v96, v99, v98
	v_div_fmas_f32 v96, v96, v97, v99
	v_div_fixup_f32 v95, v96, v94, 1.0
	v_mul_f32_e32 v18, 0x43000000, v18
	v_sub_f32_e32 v2, v2, v18
	v_sub_f32_e32 v3, v3, v18
	v_sub_f32_e32 v4, v4, v18
	v_sub_f32_e32 v5, v5, v18
	v_sub_f32_e32 v6, v6, v18
	v_sub_f32_e32 v7, v7, v18
	v_sub_f32_e32 v8, v8, v18
	v_sub_f32_e32 v9, v9, v18
	v_sub_f32_e32 v10, v10, v18
	v_sub_f32_e32 v11, v11, v18
	v_sub_f32_e32 v12, v12, v18
	v_sub_f32_e32 v13, v13, v18
	v_sub_f32_e32 v14, v14, v18
	v_sub_f32_e32 v15, v15, v18
	v_sub_f32_e32 v16, v16, v18
	v_sub_f32_e32 v17, v17, v18
	v_mul_f32_e32 v2, v95, v2
	v_mul_f32_e32 v3, v95, v3
	v_mul_f32_e32 v4, v95, v4
	v_mul_f32_e32 v5, v95, v5
	v_mul_f32_e32 v6, v95, v6
	v_mul_f32_e32 v7, v95, v7
	v_mul_f32_e32 v8, v95, v8
	v_mul_f32_e32 v9, v95, v9
	v_mul_f32_e32 v10, v95, v10
	v_mul_f32_e32 v11, v95, v11
	v_mul_f32_e32 v12, v95, v12
	v_mul_f32_e32 v13, v95, v13
	v_mul_f32_e32 v14, v95, v14
	v_mul_f32_e32 v15, v95, v15
	v_mul_f32_e32 v16, v95, v16
	v_mul_f32_e32 v17, v95, v17
	v_cvt_pk_f16_f32 v52, v2, v3
	v_cvt_pk_f16_f32 v53, v4, v5
	v_cvt_pk_f16_f32 v54, v6, v7
	v_cvt_pk_f16_f32 v55, v8, v9
	v_cvt_pk_f16_f32 v56, v10, v11
	v_cvt_pk_f16_f32 v57, v12, v13
	v_cvt_pk_f16_f32 v58, v14, v15
	v_cvt_pk_f16_f32 v59, v16, v17
	ds_write_b128 v93, v[52:55]
	ds_write_b128 v93, v[56:59] offset:16
	s_add_u32 s39, s39, 1
	s_cmp_lt_u32 s39, 2
	s_cbranch_scc1 .Lg1_set_top
	v_lshlrev_b32_e32 v107, 9, v105
	v_xor_b32_e32 v108, v106, v105
	v_lshlrev_b32_e32 v108, 4, v108
	v_mul_u32_u24_e32 v109, 0x110, v105
	v_lshl_add_u32 v109, v106, 4, v109
	v_add_u32_e32 v109, s48, v109
	v_lshlrev_b32_e32 v110, 4, v106
	v_add_u32_e32 v110, 0x10000, v110
	s_waitcnt lgkmcnt(0)
	ds_read_b128 v[52:55], v110 offset:0
	ds_read_b128 v[56:59], v110 offset:64
	ds_read_b128 v[60:63], v110 offset:128
	ds_read_b128 v[64:67], v110 offset:192
	ds_read_b128 v[68:71], v110 offset:256
	ds_read_b128 v[72:75], v110 offset:320
	ds_read_b128 v[76:79], v110 offset:384
	ds_read_b128 v[80:83], v110 offset:448
	v_xor_b32_e32 v111, 0, v108
	v_add_u32_e32 v111, v111, v107
	ds_read_b128 v[16:19], v109 offset:0
	ds_read_b128 v[84:87], v111 offset:0
	ds_read_b128 v[88:91], v111 offset:8192
	ds_read_b128 v[92:95], v111 offset:16384
	ds_read_b128 v[96:99], v111 offset:24576
	ds_read_b128 v[0:3], v111 offset:32768
	ds_read_b128 v[4:7], v111 offset:40960
	ds_read_b128 v[8:11], v111 offset:49152
	ds_read_b128 v[12:15], v111 offset:57344
	s_waitcnt lgkmcnt(0)
	v_mfma_f32_16x16x32_f16 v[52:55], v[84:87], v[16:19], v[52:55]
	v_mfma_f32_16x16x32_f16 v[56:59], v[88:91], v[16:19], v[56:59]
	v_mfma_f32_16x16x32_f16 v[60:63], v[92:95], v[16:19], v[60:63]
	v_mfma_f32_16x16x32_f16 v[64:67], v[96:99], v[16:19], v[64:67]
	v_mfma_f32_16x16x32_f16 v[68:71], v[0:3], v[16:19], v[68:71]
	v_mfma_f32_16x16x32_f16 v[72:75], v[4:7], v[16:19], v[72:75]
	v_mfma_f32_16x16x32_f16 v[76:79], v[8:11], v[16:19], v[76:79]
	v_mfma_f32_16x16x32_f16 v[80:83], v[12:15], v[16:19], v[80:83]
	v_xor_b32_e32 v111, 64, v108
	v_add_u32_e32 v111, v111, v107
	ds_read_b128 v[100:103], v109 offset:64
	ds_read_b128 v[84:87], v111 offset:0
	ds_read_b128 v[88:91], v111 offset:8192
	ds_read_b128 v[92:95], v111 offset:16384
	ds_read_b128 v[96:99], v111 offset:24576
	ds_read_b128 v[0:3], v111 offset:32768
	ds_read_b128 v[4:7], v111 offset:40960
	ds_read_b128 v[8:11], v111 offset:49152
	ds_read_b128 v[12:15], v111 offset:57344
	s_waitcnt lgkmcnt(0)
	v_mfma_f32_16x16x32_f16 v[52:55], v[84:87], v[100:103], v[52:55]
	v_mfma_f32_16x16x32_f16 v[56:59], v[88:91], v[100:103], v[56:59]
	v_mfma_f32_16x16x32_f16 v[60:63], v[92:95], v[100:103], v[60:63]
	v_mfma_f32_16x16x32_f16 v[64:67], v[96:99], v[100:103], v[64:67]
	v_mfma_f32_16x16x32_f16 v[68:71], v[0:3], v[100:103], v[68:71]
	v_mfma_f32_16x16x32_f16 v[72:75], v[4:7], v[100:103], v[72:75]
	v_mfma_f32_16x16x32_f16 v[76:79], v[8:11], v[100:103], v[76:79]
	v_mfma_f32_16x16x32_f16 v[80:83], v[12:15], v[100:103], v[80:83]
	v_xor_b32_e32 v111, 128, v108
	v_add_u32_e32 v111, v111, v107
	ds_read_b128 v[16:19], v109 offset:128
	ds_read_b128 v[84:87], v111 offset:0
	ds_read_b128 v[88:91], v111 offset:8192
	ds_read_b128 v[92:95], v111 offset:16384
	ds_read_b128 v[96:99], v111 offset:24576
	ds_read_b128 v[0:3], v111 offset:32768
	ds_read_b128 v[4:7], v111 offset:40960
	ds_read_b128 v[8:11], v111 offset:49152
	ds_read_b128 v[12:15], v111 offset:57344
	s_waitcnt lgkmcnt(0)
	v_mfma_f32_16x16x32_f16 v[52:55], v[84:87], v[16:19], v[52:55]
	v_mfma_f32_16x16x32_f16 v[56:59], v[88:91], v[16:19], v[56:59]
	v_mfma_f32_16x16x32_f16 v[60:63], v[92:95], v[16:19], v[60:63]
	v_mfma_f32_16x16x32_f16 v[64:67], v[96:99], v[16:19], v[64:67]
	v_mfma_f32_16x16x32_f16 v[68:71], v[0:3], v[16:19], v[68:71]
	v_mfma_f32_16x16x32_f16 v[72:75], v[4:7], v[16:19], v[72:75]
	v_mfma_f32_16x16x32_f16 v[76:79], v[8:11], v[16:19], v[76:79]
	v_mfma_f32_16x16x32_f16 v[80:83], v[12:15], v[16:19], v[80:83]
	v_xor_b32_e32 v111, 192, v108
	v_add_u32_e32 v111, v111, v107
	ds_read_b128 v[100:103], v109 offset:192
	ds_read_b128 v[84:87], v111 offset:0
	ds_read_b128 v[88:91], v111 offset:8192
	ds_read_b128 v[92:95], v111 offset:16384
	ds_read_b128 v[96:99], v111 offset:24576
	ds_read_b128 v[0:3], v111 offset:32768
	ds_read_b128 v[4:7], v111 offset:40960
	ds_read_b128 v[8:11], v111 offset:49152
	ds_read_b128 v[12:15], v111 offset:57344
	s_waitcnt lgkmcnt(0)
	v_mfma_f32_16x16x32_f16 v[52:55], v[84:87], v[100:103], v[52:55]
	v_mfma_f32_16x16x32_f16 v[56:59], v[88:91], v[100:103], v[56:59]
	v_mfma_f32_16x16x32_f16 v[60:63], v[92:95], v[100:103], v[60:63]
	v_mfma_f32_16x16x32_f16 v[64:67], v[96:99], v[100:103], v[64:67]
	v_mfma_f32_16x16x32_f16 v[68:71], v[0:3], v[100:103], v[68:71]
	v_mfma_f32_16x16x32_f16 v[72:75], v[4:7], v[100:103], v[72:75]
	v_mfma_f32_16x16x32_f16 v[76:79], v[8:11], v[100:103], v[76:79]
	v_mfma_f32_16x16x32_f16 v[80:83], v[12:15], v[100:103], v[80:83]
	s_waitcnt vmcnt(0)
	v_cvt_pk_f16_f32 v112, v20, v21
	v_cvt_pk_f16_f32 v113, v22, v23
	v_cvt_pk_f16_f32 v114, v24, v25
	v_cvt_pk_f16_f32 v115, v26, v27
	v_cvt_pk_f16_f32 v116, v28, v29
	v_cvt_pk_f16_f32 v117, v30, v31
	v_cvt_pk_f16_f32 v118, v32, v33
	v_cvt_pk_f16_f32 v119, v34, v35
	v_cvt_pk_f16_f32 v120, v36, v37
	v_cvt_pk_f16_f32 v121, v38, v39
	v_cvt_pk_f16_f32 v122, v40, v41
	v_cvt_pk_f16_f32 v123, v42, v43
	v_cvt_pk_f16_f32 v124, v44, v45
	v_cvt_pk_f16_f32 v125, v46, v47
	v_cvt_pk_f16_f32 v126, v48, v49
	v_cvt_pk_f16_f32 v127, v50, v51
	v_xor_b32_e32 v111, 256, v108
	v_add_u32_e32 v111, v111, v107
	ds_read_b128 v[84:87], v111 offset:0
	ds_read_b128 v[88:91], v111 offset:8192
	ds_read_b128 v[92:95], v111 offset:16384
	ds_read_b128 v[96:99], v111 offset:24576
	ds_read_b128 v[0:3], v111 offset:32768
	ds_read_b128 v[4:7], v111 offset:40960
	ds_read_b128 v[8:11], v111 offset:49152
	ds_read_b128 v[12:15], v111 offset:57344
	s_waitcnt lgkmcnt(0)
	v_xor_b32_e32 v111, 320, v108
	v_add_u32_e32 v111, v111, v107
	ds_read_b128 v[20:23], v111 offset:0
	ds_read_b128 v[24:27], v111 offset:8192
	ds_read_b128 v[28:31], v111 offset:16384
	ds_read_b128 v[32:35], v111 offset:24576
	ds_read_b128 v[36:39], v111 offset:32768
	ds_read_b128 v[40:43], v111 offset:40960
	ds_read_b128 v[44:47], v111 offset:49152
	ds_read_b128 v[48:51], v111 offset:57344
	v_mfma_f32_16x16x32_f16 v[52:55], v[84:87], v[112:115], v[52:55]
	v_mfma_f32_16x16x32_f16 v[56:59], v[88:91], v[112:115], v[56:59]
	v_mfma_f32_16x16x32_f16 v[60:63], v[92:95], v[112:115], v[60:63]
	v_mfma_f32_16x16x32_f16 v[64:67], v[96:99], v[112:115], v[64:67]
	v_mfma_f32_16x16x32_f16 v[68:71], v[0:3], v[112:115], v[68:71]
	v_mfma_f32_16x16x32_f16 v[72:75], v[4:7], v[112:115], v[72:75]
	v_mfma_f32_16x16x32_f16 v[76:79], v[8:11], v[112:115], v[76:79]
	v_mfma_f32_16x16x32_f16 v[80:83], v[12:15], v[112:115], v[80:83]
	s_waitcnt lgkmcnt(0)
	v_xor_b32_e32 v111, 384, v108
	v_add_u32_e32 v111, v111, v107
	ds_read_b128 v[84:87], v111 offset:0
	ds_read_b128 v[88:91], v111 offset:8192
	ds_read_b128 v[92:95], v111 offset:16384
	ds_read_b128 v[96:99], v111 offset:24576
	ds_read_b128 v[0:3], v111 offset:32768
	ds_read_b128 v[4:7], v111 offset:40960
	ds_read_b128 v[8:11], v111 offset:49152
	ds_read_b128 v[12:15], v111 offset:57344
	v_mfma_f32_16x16x32_f16 v[52:55], v[20:23], v[116:119], v[52:55]
	v_mfma_f32_16x16x32_f16 v[56:59], v[24:27], v[116:119], v[56:59]
	v_mfma_f32_16x16x32_f16 v[60:63], v[28:31], v[116:119], v[60:63]
	v_mfma_f32_16x16x32_f16 v[64:67], v[32:35], v[116:119], v[64:67]
	v_mfma_f32_16x16x32_f16 v[68:71], v[36:39], v[116:119], v[68:71]
	v_mfma_f32_16x16x32_f16 v[72:75], v[40:43], v[116:119], v[72:75]
	v_mfma_f32_16x16x32_f16 v[76:79], v[44:47], v[116:119], v[76:79]
	v_mfma_f32_16x16x32_f16 v[80:83], v[48:51], v[116:119], v[80:83]
	s_waitcnt lgkmcnt(0)
	v_xor_b32_e32 v111, 448, v108
	v_add_u32_e32 v111, v111, v107
	ds_read_b128 v[20:23], v111 offset:0
	ds_read_b128 v[24:27], v111 offset:8192
	ds_read_b128 v[28:31], v111 offset:16384
	ds_read_b128 v[32:35], v111 offset:24576
	ds_read_b128 v[36:39], v111 offset:32768
	ds_read_b128 v[40:43], v111 offset:40960
	ds_read_b128 v[44:47], v111 offset:49152
	ds_read_b128 v[48:51], v111 offset:57344
	v_mfma_f32_16x16x32_f16 v[52:55], v[84:87], v[120:123], v[52:55]
	v_mfma_f32_16x16x32_f16 v[56:59], v[88:91], v[120:123], v[56:59]
	v_mfma_f32_16x16x32_f16 v[60:63], v[92:95], v[120:123], v[60:63]
	v_mfma_f32_16x16x32_f16 v[64:67], v[96:99], v[120:123], v[64:67]
	v_mfma_f32_16x16x32_f16 v[68:71], v[0:3], v[120:123], v[68:71]
	v_mfma_f32_16x16x32_f16 v[72:75], v[4:7], v[120:123], v[72:75]
	v_mfma_f32_16x16x32_f16 v[76:79], v[8:11], v[120:123], v[76:79]
	v_mfma_f32_16x16x32_f16 v[80:83], v[12:15], v[120:123], v[80:83]
	s_waitcnt lgkmcnt(0)
	v_mfma_f32_16x16x32_f16 v[52:55], v[20:23], v[124:127], v[52:55]
	v_mfma_f32_16x16x32_f16 v[56:59], v[24:27], v[124:127], v[56:59]
	v_mfma_f32_16x16x32_f16 v[60:63], v[28:31], v[124:127], v[60:63]
	v_mfma_f32_16x16x32_f16 v[64:67], v[32:35], v[124:127], v[64:67]
	v_mfma_f32_16x16x32_f16 v[68:71], v[36:39], v[124:127], v[68:71]
	v_mfma_f32_16x16x32_f16 v[72:75], v[40:43], v[124:127], v[72:75]
	v_mfma_f32_16x16x32_f16 v[76:79], v[44:47], v[124:127], v[76:79]
	v_mfma_f32_16x16x32_f16 v[80:83], v[48:51], v[124:127], v[80:83]
	s_nop 7
	s_nop 3
	v_max_f32_e32 v52, 0, v52
	v_max_f32_e32 v53, 0, v53
	v_max_f32_e32 v54, 0, v54
	v_max_f32_e32 v55, 0, v55
	v_max_f32_e32 v56, 0, v56
	v_max_f32_e32 v57, 0, v57
	v_max_f32_e32 v58, 0, v58
	v_max_f32_e32 v59, 0, v59
	v_max_f32_e32 v60, 0, v60
	v_max_f32_e32 v61, 0, v61
	v_max_f32_e32 v62, 0, v62
	v_max_f32_e32 v63, 0, v63
	v_max_f32_e32 v64, 0, v64
	v_max_f32_e32 v65, 0, v65
	v_max_f32_e32 v66, 0, v66
	v_max_f32_e32 v67, 0, v67
	v_max_f32_e32 v68, 0, v68
	v_max_f32_e32 v69, 0, v69
	v_max_f32_e32 v70, 0, v70
	v_max_f32_e32 v71, 0, v71
	v_max_f32_e32 v72, 0, v72
	v_max_f32_e32 v73, 0, v73
	v_max_f32_e32 v74, 0, v74
	v_max_f32_e32 v75, 0, v75
	v_max_f32_e32 v76, 0, v76
	v_max_f32_e32 v77, 0, v77
	v_max_f32_e32 v78, 0, v78
	v_max_f32_e32 v79, 0, v79
	v_max_f32_e32 v80, 0, v80
	v_max_f32_e32 v81, 0, v81
	v_max_f32_e32 v82, 0, v82
	v_max_f32_e32 v83, 0, v83
	v_max3_f32 v1, v52, v53, v54
	v_max3_f32 v1, v1, v55, v56
	v_max3_f32 v1, v1, v57, v58
	v_max3_f32 v1, v1, v59, v60
	v_max3_f32 v1, v1, v61, v62
	v_max3_f32 v1, v1, v63, v64
	v_max3_f32 v1, v1, v65, v66
	v_max3_f32 v1, v1, v67, v68
	v_max3_f32 v1, v1, v69, v70
	v_max3_f32 v1, v1, v71, v72
	v_max3_f32 v1, v1, v73, v74
	v_max3_f32 v1, v1, v75, v76
	v_max3_f32 v1, v1, v77, v78
	v_max3_f32 v1, v1, v79, v80
	v_max3_f32 v1, v1, v81, v82
	v_max_f32_e32 v1, v1, v83
	v_lshl_or_b32 v0, v106, 4, v105
	v_xor_b32_e32 v2, 16, v0
	v_lshlrev_b32_e32 v2, 2, v2
	ds_bpermute_b32 v3, v2, v1
	s_waitcnt lgkmcnt(0)
	v_max_f32_e32 v1, v1, v3
	v_xor_b32_e32 v2, 32, v0
	v_lshlrev_b32_e32 v2, 2, v2
	ds_bpermute_b32 v3, v2, v1
	s_waitcnt lgkmcnt(0)
	v_max_f32_e32 v1, v1, v3
	s_mov_b32 s58, 0x437f0000
	v_div_scale_f32 v5, s[62:63], v1, v1, s58
	v_rcp_f32_e32 v6, v5
	v_div_scale_f32 v7, vcc, s58, v1, s58
	v_fma_f32 v8, -v5, v6, 1.0
	v_fmac_f32_e32 v6, v8, v6
	v_mul_f32_e32 v8, v7, v6
	v_fma_f32 v4, -v5, v8, v7
	v_fmac_f32_e32 v8, v4, v6
	v_fma_f32 v5, -v5, v8, v7
	v_div_fmas_f32 v5, v5, v6, v8
	v_div_fixup_f32 v4, v5, v1, s58
	v_cmp_lt_f32_e32 vcc, 0, v1
	s_nop 1
	v_cndmask_b32_e32 v4, 0, v4, vcc
	v_mul_u32_u24_e32 v9, 0x110, v105
	v_lshl_add_u32 v9, v106, 3, v9
	v_add_u32_e32 v9, s48, v9
	v_mul_u32_u24_e32 v10, 0x110, v106
	v_lshl_add_u32 v10, v105, 4, v10
	v_add_u32_e32 v10, s48, v10
	v_mul_u32_u24_e32 v11, 0x90, v105
	v_lshl_add_u32 v11, v106, 2, v11
	v_add_u32_e32 v11, s48, v11
	v_lshrrev_b32_e32 v14, 3, v0
	v_and_b32_e32 v16, 7, v0
	v_mul_u32_u24_e32 v12, 0x90, v14
	v_lshl_add_u32 v12, v16, 4, v12
	v_add_u32_e32 v12, s48, v12
	v_lshlrev_b32_e32 v14, 2, v14
	v_lshlrev_b32_e32 v16, 4, v16
	v_lshlrev_b32_e32 v13, 2, v106
	v_lshlrev_b32_e32 v15, 4, v105
	ds_bpermute_b32 v20, v13, v104 offset:0
	ds_bpermute_b32 v21, v13, v104 offset:16
	ds_bpermute_b32 v22, v13, v104 offset:32
	ds_bpermute_b32 v23, v13, v104 offset:48
	ds_bpermute_b32 v24, v14, v104 offset:0
	ds_bpermute_b32 v25, v14, v104 offset:32
	s_waitcnt lgkmcnt(0)
	v_cvt_pk_f16_f32 v26, v52, v53
	v_cvt_pk_f16_f32 v27, v54, v55
	ds_write_b64 v9, v[26:27] offset:0
	v_cvt_pk_f16_f32 v26, v56, v57
	v_cvt_pk_f16_f32 v27, v58, v59
	ds_write_b64 v9, v[26:27] offset:32
	v_cvt_pk_f16_f32 v26, v60, v61
	v_cvt_pk_f16_f32 v27, v62, v63
	ds_write_b64 v9, v[26:27] offset:64
	v_cvt_pk_f16_f32 v26, v64, v65
	v_cvt_pk_f16_f32 v27, v66, v67
	ds_write_b64 v9, v[26:27] offset:96
	v_cvt_pk_f16_f32 v26, v68, v69
	v_cvt_pk_f16_f32 v27, v70, v71
	ds_write_b64 v9, v[26:27] offset:128
	v_cvt_pk_f16_f32 v26, v72, v73
	v_cvt_pk_f16_f32 v27, v74, v75
	ds_write_b64 v9, v[26:27] offset:160
	v_cvt_pk_f16_f32 v26, v76, v77
	v_cvt_pk_f16_f32 v27, v78, v79
	ds_write_b64 v9, v[26:27] offset:192
	v_cvt_pk_f16_f32 v26, v80, v81
	v_cvt_pk_f16_f32 v27, v82, v83
	ds_write_b64 v9, v[26:27] offset:224
	ds_read_b128 v[28:31], v10 offset:0
	ds_read_b128 v[32:35], v10 offset:1088
	ds_read_b128 v[36:39], v10 offset:2176
	ds_read_b128 v[40:43], v10 offset:3264
	s_waitcnt lgkmcnt(3)
	v_lshl_or_b32 v20, v20, 8, v15
	global_store_dwordx4 v20, v[28:31], s[26:27] sc1
	s_waitcnt lgkmcnt(2)
	v_lshl_or_b32 v21, v21, 8, v15
	global_store_dwordx4 v21, v[32:35], s[26:27] sc1
	s_waitcnt lgkmcnt(1)
	v_lshl_or_b32 v22, v22, 8, v15
	global_store_dwordx4 v22, v[36:39], s[26:27] sc1
	s_waitcnt lgkmcnt(0)
	v_lshl_or_b32 v23, v23, 8, v15
	global_store_dwordx4 v23, v[40:43], s[26:27] sc1
	v_mul_f32_e32 v44, v4, v52
	v_mul_f32_e32 v45, v4, v53
	v_mul_f32_e32 v46, v4, v54
	v_mul_f32_e32 v47, v4, v55
	v_rndne_f32_e32 v44, v44
	v_rndne_f32_e32 v45, v45
	v_rndne_f32_e32 v46, v46
	v_rndne_f32_e32 v47, v47
	v_cvt_i32_f32_e32 v44, v44
	v_cvt_i32_f32_e32 v45, v45
	v_cvt_i32_f32_e32 v46, v46
	v_cvt_i32_f32_e32 v47, v47
	v_lshl_or_b32 v44, v45, 8, v44
	v_lshl_or_b32 v44, v46, 16, v44
	v_lshl_or_b32 v44, v47, 24, v44
	ds_write_b32 v11, v44 offset:0
	v_mul_f32_e32 v44, v4, v56
	v_mul_f32_e32 v45, v4, v57
	v_mul_f32_e32 v46, v4, v58
	v_mul_f32_e32 v47, v4, v59
	v_rndne_f32_e32 v44, v44
	v_rndne_f32_e32 v45, v45
	v_rndne_f32_e32 v46, v46
	v_rndne_f32_e32 v47, v47
	v_cvt_i32_f32_e32 v44, v44
	v_cvt_i32_f32_e32 v45, v45
	v_cvt_i32_f32_e32 v46, v46
	v_cvt_i32_f32_e32 v47, v47
	v_lshl_or_b32 v44, v45, 8, v44
	v_lshl_or_b32 v44, v46, 16, v44
	v_lshl_or_b32 v44, v47, 24, v44
	ds_write_b32 v11, v44 offset:16
	v_mul_f32_e32 v44, v4, v60
	v_mul_f32_e32 v45, v4, v61
	v_mul_f32_e32 v46, v4, v62
	v_mul_f32_e32 v47, v4, v63
	v_rndne_f32_e32 v44, v44
	v_rndne_f32_e32 v45, v45
	v_rndne_f32_e32 v46, v46
	v_rndne_f32_e32 v47, v47
	v_cvt_i32_f32_e32 v44, v44
	v_cvt_i32_f32_e32 v45, v45
	v_cvt_i32_f32_e32 v46, v46
	v_cvt_i32_f32_e32 v47, v47
	v_lshl_or_b32 v44, v45, 8, v44
	v_lshl_or_b32 v44, v46, 16, v44
	v_lshl_or_b32 v44, v47, 24, v44
	ds_write_b32 v11, v44 offset:32
	v_mul_f32_e32 v44, v4, v64
	v_mul_f32_e32 v45, v4, v65
	v_mul_f32_e32 v46, v4, v66
	v_mul_f32_e32 v47, v4, v67
	v_rndne_f32_e32 v44, v44
	v_rndne_f32_e32 v45, v45
	v_rndne_f32_e32 v46, v46
	v_rndne_f32_e32 v47, v47
	v_cvt_i32_f32_e32 v44, v44
	v_cvt_i32_f32_e32 v45, v45
	v_cvt_i32_f32_e32 v46, v46
	v_cvt_i32_f32_e32 v47, v47
	v_lshl_or_b32 v44, v45, 8, v44
	v_lshl_or_b32 v44, v46, 16, v44
	v_lshl_or_b32 v44, v47, 24, v44
	ds_write_b32 v11, v44 offset:48
	v_mul_f32_e32 v44, v4, v68
	v_mul_f32_e32 v45, v4, v69
	v_mul_f32_e32 v46, v4, v70
	v_mul_f32_e32 v47, v4, v71
	v_rndne_f32_e32 v44, v44
	v_rndne_f32_e32 v45, v45
	v_rndne_f32_e32 v46, v46
	v_rndne_f32_e32 v47, v47
	v_cvt_i32_f32_e32 v44, v44
	v_cvt_i32_f32_e32 v45, v45
	v_cvt_i32_f32_e32 v46, v46
	v_cvt_i32_f32_e32 v47, v47
	v_lshl_or_b32 v44, v45, 8, v44
	v_lshl_or_b32 v44, v46, 16, v44
	v_lshl_or_b32 v44, v47, 24, v44
	ds_write_b32 v11, v44 offset:64
	v_mul_f32_e32 v44, v4, v72
	v_mul_f32_e32 v45, v4, v73
	v_mul_f32_e32 v46, v4, v74
	v_mul_f32_e32 v47, v4, v75
	v_rndne_f32_e32 v44, v44
	v_rndne_f32_e32 v45, v45
	v_rndne_f32_e32 v46, v46
	v_rndne_f32_e32 v47, v47
	v_cvt_i32_f32_e32 v44, v44
	v_cvt_i32_f32_e32 v45, v45
	v_cvt_i32_f32_e32 v46, v46
	v_cvt_i32_f32_e32 v47, v47
	v_lshl_or_b32 v44, v45, 8, v44
	v_lshl_or_b32 v44, v46, 16, v44
	v_lshl_or_b32 v44, v47, 24, v44
	ds_write_b32 v11, v44 offset:80
	v_mul_f32_e32 v44, v4, v76
	v_mul_f32_e32 v45, v4, v77
	v_mul_f32_e32 v46, v4, v78
	v_mul_f32_e32 v47, v4, v79
	v_rndne_f32_e32 v44, v44
	v_rndne_f32_e32 v45, v45
	v_rndne_f32_e32 v46, v46
	v_rndne_f32_e32 v47, v47
	v_cvt_i32_f32_e32 v44, v44
	v_cvt_i32_f32_e32 v45, v45
	v_cvt_i32_f32_e32 v46, v46
	v_cvt_i32_f32_e32 v47, v47
	v_lshl_or_b32 v44, v45, 8, v44
	v_lshl_or_b32 v44, v46, 16, v44
	v_lshl_or_b32 v44, v47, 24, v44
	ds_write_b32 v11, v44 offset:96
	v_mul_f32_e32 v44, v4, v80
	v_mul_f32_e32 v45, v4, v81
	v_mul_f32_e32 v46, v4, v82
	v_mul_f32_e32 v47, v4, v83
	v_rndne_f32_e32 v44, v44
	v_rndne_f32_e32 v45, v45
	v_rndne_f32_e32 v46, v46
	v_rndne_f32_e32 v47, v47
	v_cvt_i32_f32_e32 v44, v44
	v_cvt_i32_f32_e32 v45, v45
	v_cvt_i32_f32_e32 v46, v46
	v_cvt_i32_f32_e32 v47, v47
	v_lshl_or_b32 v44, v45, 8, v44
	v_lshl_or_b32 v44, v46, 16, v44
	v_lshl_or_b32 v44, v47, 24, v44
	ds_write_b32 v11, v44 offset:112
	ds_read_b128 v[84:87], v12 offset:0
	ds_read_b128 v[88:91], v12 offset:1152
	s_waitcnt lgkmcnt(1)
	v_lshl_or_b32 v24, v24, 7, v16
	global_store_dwordx4 v24, v[84:87], s[28:29] sc1
	s_waitcnt lgkmcnt(0)
	v_lshl_or_b32 v25, v25, 7, v16
	global_store_dwordx4 v25, v[88:91], s[28:29] sc1
	v_cmp_eq_u32_e32 vcc, 0, v106
	s_and_saveexec_b64 s[44:45], vcc
	s_mov_b32 s58, 0x3b808081
	v_fma_mixlo_f16 v2, v1, s58, 0
	v_lshlrev_b32_e32 v3, 1, v104
	global_store_short v3, v2, s[30:31]
	s_endpgm
	.p2alignl 8, 3212836864
